# pipelined diff-attention with packed f32 row-sum adds
# speedup vs baseline: 1.0053x; 1.0006x over previous
.Lattn_noresc0_a:
	ds_read_b64_tr_b16 v[156:157], v215 offset:36864
	ds_read_b64_tr_b16 v[158:159], v215 offset:38912
	ds_read_b64_tr_b16 v[192:193], v212 offset:40960
	ds_read_b64_tr_b16 v[194:195], v212 offset:43008
	ds_read_b64_tr_b16 v[196:197], v213 offset:40960
	ds_read_b64_tr_b16 v[198:199], v213 offset:43008
	ds_read_b64_tr_b16 v[200:201], v214 offset:40960
	ds_read_b64_tr_b16 v[202:203], v214 offset:43008
	v_sub_f32_e32 v160, v160, v229
	v_sub_f32_e32 v161, v161, v229
	v_sub_f32_e32 v162, v162, v229
	s_waitcnt lgkmcnt(12)
	v_mfma_f32_32x32x16_bf16 v[112:127], v[132:135], v[144:147], v[112:127]
	ds_read_b64_tr_b16 v[204:205], v215 offset:40960
	ds_read_b64_tr_b16 v[206:207], v215 offset:43008
	v_sub_f32_e32 v163, v163, v229
	v_exp_f32_e32 v160, v160
	v_exp_f32_e32 v161, v161
	v_exp_f32_e32 v162, v162
	s_waitcnt lgkmcnt(12)
	v_mfma_f32_32x32x16_bf16 v[96:111], v[132:135], v[148:151], v[96:111]
	ds_read_b64_tr_b16 v[144:145], v212 offset:45056
	ds_read_b64_tr_b16 v[146:147], v212 offset:47104
	v_exp_f32_e32 v163, v163
	v_sub_f32_e32 v164, v164, v229
	v_sub_f32_e32 v165, v165, v229
	v_sub_f32_e32 v166, v166, v229
	s_waitcnt lgkmcnt(12)
	v_mfma_f32_32x32x16_bf16 v[80:95], v[132:135], v[152:155], v[80:95]
	ds_read_b64_tr_b16 v[148:149], v213 offset:45056
	ds_read_b64_tr_b16 v[150:151], v213 offset:47104
	v_sub_f32_e32 v167, v167, v229
	v_exp_f32_e32 v164, v164
	v_exp_f32_e32 v165, v165
	v_exp_f32_e32 v166, v166
	v_exp_f32_e32 v167, v167
	s_waitcnt lgkmcnt(12)
	v_mfma_f32_32x32x16_bf16 v[48:63], v[132:135], v[156:159], v[48:63]
	ds_read_b64_tr_b16 v[152:153], v214 offset:45056
	ds_read_b64_tr_b16 v[154:155], v214 offset:47104
	v_pk_add_f32 v[254:255], v[160:161], v[162:163]
	v_cvt_pk_bf16_f32 v160, v160, v161
	v_cvt_pk_bf16_f32 v161, v162, v163
	v_sub_f32_e32 v168, v168, v229
	s_waitcnt lgkmcnt(12)
	v_mfma_f32_32x32x16_bf16 v[112:127], v[136:139], v[192:195], v[112:127]
	ds_read_b64_tr_b16 v[156:157], v215 offset:45056
	ds_read_b64_tr_b16 v[158:159], v215 offset:47104
	v_sub_f32_e32 v169, v169, v229
	v_sub_f32_e32 v170, v170, v229
	v_sub_f32_e32 v171, v171, v229
	v_exp_f32_e32 v168, v168
	v_exp_f32_e32 v169, v169
	s_waitcnt lgkmcnt(12)
	v_mfma_f32_32x32x16_bf16 v[96:111], v[136:139], v[196:199], v[96:111]
	v_add_u32_e32 v230, v236, v244
	ds_read_b128 v[192:195], v230
	v_exp_f32_e32 v170, v170
	v_exp_f32_e32 v171, v171
	v_pk_add_f32 v[254:255], v[254:255], v[164:165]
	v_pk_add_f32 v[254:255], v[254:255], v[166:167]
	s_waitcnt lgkmcnt(11)
	v_mfma_f32_32x32x16_bf16 v[80:95], v[136:139], v[200:203], v[80:95]
	v_add3_u32 v230, v237, v244, s48
	ds_read_b128 v[196:199], v230
	v_cvt_pk_bf16_f32 v162, v164, v165
	v_cvt_pk_bf16_f32 v163, v166, v167
	v_sub_f32_e32 v172, v172, v229
	v_sub_f32_e32 v173, v173, v229
	v_sub_f32_e32 v174, v174, v229
	s_waitcnt lgkmcnt(10)
	v_mfma_f32_32x32x16_bf16 v[48:63], v[136:139], v[204:207], v[48:63]
	v_add3_u32 v230, v237, v244, s48
	ds_read_b128 v[200:203], v230 offset:8192
	v_sub_f32_e32 v175, v175, v229
	v_exp_f32_e32 v172, v172
	v_exp_f32_e32 v173, v173
	v_exp_f32_e32 v174, v174
	s_waitcnt lgkmcnt(9)
	v_mfma_f32_32x32x16_bf16 v[112:127], v[140:143], v[144:147], v[112:127]
	v_add_u32_e32 v230, v236, v245
	ds_read_b128 v[204:207], v230
	v_exp_f32_e32 v175, v175
	v_pk_add_f32 v[254:255], v[254:255], v[168:169]
	v_pk_add_f32 v[254:255], v[254:255], v[170:171]
	v_cvt_pk_bf16_f32 v164, v168, v169
	v_cvt_pk_bf16_f32 v165, v170, v171
	s_waitcnt lgkmcnt(8)
	v_mfma_f32_32x32x16_bf16 v[96:111], v[140:143], v[148:151], v[96:111]
	v_sub_f32_e32 v176, v176, v229
	v_sub_f32_e32 v177, v177, v229
	v_sub_f32_e32 v178, v178, v229
	v_sub_f32_e32 v179, v179, v229
	s_waitcnt lgkmcnt(6)
	v_mfma_f32_32x32x16_bf16 v[80:95], v[140:143], v[152:155], v[80:95]
	v_exp_f32_e32 v176, v176
	v_exp_f32_e32 v177, v177
	v_exp_f32_e32 v178, v178
	v_exp_f32_e32 v179, v179
	v_pk_add_f32 v[254:255], v[254:255], v[172:173]
	s_waitcnt lgkmcnt(4)
	v_mfma_f32_32x32x16_bf16 v[48:63], v[140:143], v[156:159], v[48:63]
	v_pk_add_f32 v[254:255], v[254:255], v[174:175]
	v_cvt_pk_bf16_f32 v166, v172, v173
	v_cvt_pk_bf16_f32 v167, v174, v175
	v_sub_f32_e32 v180, v180, v229
	s_waitcnt lgkmcnt(2)
	v_mfma_f32_32x32x16_bf16 v[128:143], v[196:199], v[192:195], 0
	v_add3_u32 v230, v237, v245, s48
	ds_read_b128 v[196:199], v230
	v_sub_f32_e32 v181, v181, v229
	v_sub_f32_e32 v182, v182, v229
	v_sub_f32_e32 v183, v183, v229
	v_exp_f32_e32 v180, v180
	s_waitcnt lgkmcnt(2)
	v_mfma_f32_32x32x16_bf16 v[144:159], v[200:203], v[192:195], 0
	v_add3_u32 v230, v237, v245, s48
	ds_read_b128 v[200:203], v230 offset:8192
	v_add_u32_e32 v230, v236, v246
	ds_read_b128 v[192:195], v230
	v_exp_f32_e32 v181, v181
	v_exp_f32_e32 v182, v182
	v_exp_f32_e32 v183, v183
	v_pk_add_f32 v[254:255], v[254:255], v[176:177]
	v_pk_add_f32 v[254:255], v[254:255], v[178:179]
	s_waitcnt lgkmcnt(2)
	v_mfma_f32_32x32x16_bf16 v[128:143], v[196:199], v[204:207], v[128:143]
	v_add3_u32 v230, v237, v246, s48
	ds_read_b128 v[196:199], v230
	v_cvt_pk_bf16_f32 v168, v176, v177
	v_cvt_pk_bf16_f32 v169, v178, v179
	v_sub_f32_e32 v184, v184, v229
	v_sub_f32_e32 v185, v185, v229
	s_waitcnt lgkmcnt(2)
	v_mfma_f32_32x32x16_bf16 v[144:159], v[200:203], v[204:207], v[144:159]
	v_add3_u32 v230, v237, v246, s48
	ds_read_b128 v[200:203], v230 offset:8192
	v_add_u32_e32 v230, v236, v247
	ds_read_b128 v[204:207], v230
	v_sub_f32_e32 v186, v186, v229
	v_sub_f32_e32 v187, v187, v229
	v_exp_f32_e32 v184, v184
	v_exp_f32_e32 v185, v185
	v_exp_f32_e32 v186, v186
	s_waitcnt lgkmcnt(2)
	v_mfma_f32_32x32x16_bf16 v[128:143], v[196:199], v[192:195], v[128:143]
	v_add3_u32 v230, v237, v247, s48
	ds_read_b128 v[196:199], v230
	v_exp_f32_e32 v187, v187
	v_pk_add_f32 v[254:255], v[254:255], v[180:181]
	v_pk_add_f32 v[254:255], v[254:255], v[182:183]
	v_cvt_pk_bf16_f32 v170, v180, v181
	s_waitcnt lgkmcnt(2)
	v_mfma_f32_32x32x16_bf16 v[144:159], v[200:203], v[192:195], v[144:159]
	v_add3_u32 v230, v237, v247, s48
	ds_read_b128 v[200:203], v230 offset:8192
	v_cvt_pk_bf16_f32 v171, v182, v183
	v_sub_f32_e32 v188, v188, v229
	v_sub_f32_e32 v189, v189, v229
	v_sub_f32_e32 v190, v190, v229
	v_sub_f32_e32 v191, v191, v229
	s_waitcnt lgkmcnt(1)
	v_mfma_f32_32x32x16_bf16 v[128:143], v[196:199], v[204:207], v[128:143]
	v_exp_f32_e32 v188, v188
	v_exp_f32_e32 v189, v189
	v_exp_f32_e32 v190, v190
	v_exp_f32_e32 v191, v191
	s_waitcnt lgkmcnt(0)
	v_mfma_f32_32x32x16_bf16 v[144:159], v[200:203], v[204:207], v[144:159]
	v_pk_add_f32 v[254:255], v[254:255], v[184:185]
	v_pk_add_f32 v[254:255], v[254:255], v[186:187]
	v_cvt_pk_bf16_f32 v172, v184, v185
	v_cvt_pk_bf16_f32 v173, v186, v187
	s_nop 0
	v_pk_add_f32 v[254:255], v[254:255], v[188:189]
	v_pk_add_f32 v[254:255], v[254:255], v[190:191]
	v_cvt_pk_bf16_f32 v174, v188, v189
	v_cvt_pk_bf16_f32 v175, v190, v191
	v_add_f32_e32 v254, v254, v255
	v_mov_b32_e32 v255, v254
	s_nop 1
	v_permlane32_swap_b32_e32 v254, v255
	v_add_f32_e32 v254, v254, v255
	v_fma_f32 v251, v251, v228, v254
	s_branch .Lattn_mid

.Lattn_noresc0_b:
	v_add_u32_e32 v230, v236, v244
	ds_read_b128 v[192:195], v230
	v_add3_u32 v230, v237, v244, s48
	ds_read_b128 v[196:199], v230
	v_add3_u32 v230, v237, v244, s48
	ds_read_b128 v[200:203], v230 offset:8192
	v_add_u32_e32 v230, v236, v245
	ds_read_b128 v[204:207], v230
	v_sub_f32_e32 v160, v160, v229
	v_sub_f32_e32 v161, v161, v229
	v_sub_f32_e32 v162, v162, v229
	s_waitcnt lgkmcnt(2)
	v_mfma_f32_32x32x16_bf16 v[128:143], v[196:199], v[192:195], 0
	v_add3_u32 v230, v237, v245, s48
	ds_read_b128 v[196:199], v230
	v_sub_f32_e32 v163, v163, v229
	v_exp_f32_e32 v160, v160
	v_exp_f32_e32 v161, v161
	v_exp_f32_e32 v162, v162
	v_exp_f32_e32 v163, v163
	v_sub_f32_e32 v164, v164, v229
	v_sub_f32_e32 v165, v165, v229
	v_sub_f32_e32 v166, v166, v229
	v_sub_f32_e32 v167, v167, v229
	v_exp_f32_e32 v164, v164
	v_exp_f32_e32 v165, v165
	v_exp_f32_e32 v166, v166
	s_waitcnt lgkmcnt(2)
	v_mfma_f32_32x32x16_bf16 v[144:159], v[200:203], v[192:195], 0
	v_add3_u32 v230, v237, v245, s48
	ds_read_b128 v[200:203], v230 offset:8192
	v_add_u32_e32 v230, v236, v246
	ds_read_b128 v[192:195], v230
	v_exp_f32_e32 v167, v167
	v_pk_add_f32 v[254:255], v[160:161], v[162:163]
	v_cvt_pk_bf16_f32 v160, v160, v161
	v_cvt_pk_bf16_f32 v161, v162, v163
	v_sub_f32_e32 v168, v168, v229
	v_sub_f32_e32 v169, v169, v229
	v_sub_f32_e32 v170, v170, v229
	v_sub_f32_e32 v171, v171, v229
	v_exp_f32_e32 v168, v168
	v_exp_f32_e32 v169, v169
	v_exp_f32_e32 v170, v170
	v_exp_f32_e32 v171, v171
	s_waitcnt lgkmcnt(2)
	v_mfma_f32_32x32x16_bf16 v[128:143], v[196:199], v[204:207], v[128:143]
	v_add3_u32 v230, v237, v246, s48
	ds_read_b128 v[196:199], v230
	v_pk_add_f32 v[254:255], v[254:255], v[164:165]
	v_pk_add_f32 v[254:255], v[254:255], v[166:167]
	v_cvt_pk_bf16_f32 v162, v164, v165
	v_cvt_pk_bf16_f32 v163, v166, v167
	v_sub_f32_e32 v172, v172, v229
	v_sub_f32_e32 v173, v173, v229
	v_sub_f32_e32 v174, v174, v229
	v_sub_f32_e32 v175, v175, v229
	v_exp_f32_e32 v172, v172
	v_exp_f32_e32 v173, v173
	v_exp_f32_e32 v174, v174
	v_exp_f32_e32 v175, v175
	s_waitcnt lgkmcnt(2)
	v_mfma_f32_32x32x16_bf16 v[144:159], v[200:203], v[204:207], v[144:159]
	v_add3_u32 v230, v237, v246, s48
	ds_read_b128 v[200:203], v230 offset:8192
	v_add_u32_e32 v230, v236, v247
	ds_read_b128 v[204:207], v230
	v_pk_add_f32 v[254:255], v[254:255], v[168:169]
	v_pk_add_f32 v[254:255], v[254:255], v[170:171]
	v_cvt_pk_bf16_f32 v164, v168, v169
	v_cvt_pk_bf16_f32 v165, v170, v171
	v_sub_f32_e32 v176, v176, v229
	v_sub_f32_e32 v177, v177, v229
	v_sub_f32_e32 v178, v178, v229
	v_sub_f32_e32 v179, v179, v229
	v_exp_f32_e32 v176, v176
	v_exp_f32_e32 v177, v177
	v_exp_f32_e32 v178, v178
	v_exp_f32_e32 v179, v179
	s_waitcnt lgkmcnt(2)
	v_mfma_f32_32x32x16_bf16 v[128:143], v[196:199], v[192:195], v[128:143]
	v_add3_u32 v230, v237, v247, s48
	ds_read_b128 v[196:199], v230
	v_pk_add_f32 v[254:255], v[254:255], v[172:173]
	v_pk_add_f32 v[254:255], v[254:255], v[174:175]
	v_cvt_pk_bf16_f32 v166, v172, v173
	v_cvt_pk_bf16_f32 v167, v174, v175
	v_sub_f32_e32 v180, v180, v229
	v_sub_f32_e32 v181, v181, v229
	v_sub_f32_e32 v182, v182, v229
	v_sub_f32_e32 v183, v183, v229
	v_exp_f32_e32 v180, v180
	v_exp_f32_e32 v181, v181
	v_exp_f32_e32 v182, v182
	v_exp_f32_e32 v183, v183
	s_waitcnt lgkmcnt(2)
	v_mfma_f32_32x32x16_bf16 v[144:159], v[200:203], v[192:195], v[144:159]
	v_add3_u32 v230, v237, v247, s48
	ds_read_b128 v[200:203], v230 offset:8192
	v_pk_add_f32 v[254:255], v[254:255], v[176:177]
	v_pk_add_f32 v[254:255], v[254:255], v[178:179]
	v_cvt_pk_bf16_f32 v168, v176, v177
	v_cvt_pk_bf16_f32 v169, v178, v179
	v_sub_f32_e32 v184, v184, v229
	v_sub_f32_e32 v185, v185, v229
	v_sub_f32_e32 v186, v186, v229
	v_sub_f32_e32 v187, v187, v229
	v_exp_f32_e32 v184, v184
	v_exp_f32_e32 v185, v185
	v_exp_f32_e32 v186, v186
	v_exp_f32_e32 v187, v187
	s_waitcnt lgkmcnt(1)
	v_mfma_f32_32x32x16_bf16 v[128:143], v[196:199], v[204:207], v[128:143]
	v_pk_add_f32 v[254:255], v[254:255], v[180:181]
	v_pk_add_f32 v[254:255], v[254:255], v[182:183]
	v_cvt_pk_bf16_f32 v170, v180, v181
	v_cvt_pk_bf16_f32 v171, v182, v183
	v_sub_f32_e32 v188, v188, v229
	v_sub_f32_e32 v189, v189, v229
	v_sub_f32_e32 v190, v190, v229
	v_sub_f32_e32 v191, v191, v229
	v_exp_f32_e32 v188, v188
	v_exp_f32_e32 v189, v189
	v_exp_f32_e32 v190, v190
	v_exp_f32_e32 v191, v191
	s_waitcnt lgkmcnt(0)
	v_mfma_f32_32x32x16_bf16 v[144:159], v[200:203], v[204:207], v[144:159]
	v_pk_add_f32 v[254:255], v[254:255], v[184:185]
	v_pk_add_f32 v[254:255], v[254:255], v[186:187]
	v_cvt_pk_bf16_f32 v172, v184, v185
	v_cvt_pk_bf16_f32 v173, v186, v187
	s_nop 0
	v_pk_add_f32 v[254:255], v[254:255], v[188:189]
	v_pk_add_f32 v[254:255], v[254:255], v[190:191]
	v_cvt_pk_bf16_f32 v174, v188, v189
	v_cvt_pk_bf16_f32 v175, v190, v191
	v_add_f32_e32 v254, v254, v255
	v_mov_b32_e32 v255, v254
	s_nop 1
	v_permlane32_swap_b32_e32 v254, v255
	v_add_f32_e32 v254, v254, v255
	v_fma_f32 v251, v251, v228, v254
	s_branch .Lattn_mid

.Lattn_noresc1_c:
	ds_read_b64_tr_b16 v[188:189], v215 offset:36864
	ds_read_b64_tr_b16 v[190:191], v215 offset:38912
	ds_read_b64_tr_b16 v[192:193], v212 offset:40960
	ds_read_b64_tr_b16 v[194:195], v212 offset:43008
	ds_read_b64_tr_b16 v[196:197], v213 offset:40960
	ds_read_b64_tr_b16 v[198:199], v213 offset:43008
	ds_read_b64_tr_b16 v[200:201], v214 offset:40960
	ds_read_b64_tr_b16 v[202:203], v214 offset:43008
	v_sub_f32_e32 v128, v128, v229
	v_sub_f32_e32 v129, v129, v229
	v_sub_f32_e32 v130, v130, v229
	s_waitcnt lgkmcnt(12)
	v_mfma_f32_32x32x16_bf16 v[64:79], v[164:167], v[176:179], v[64:79]
	ds_read_b64_tr_b16 v[204:205], v215 offset:40960
	ds_read_b64_tr_b16 v[206:207], v215 offset:43008
	v_sub_f32_e32 v131, v131, v229
	v_exp_f32_e32 v128, v128
	v_exp_f32_e32 v129, v129
	v_exp_f32_e32 v130, v130
	s_waitcnt lgkmcnt(12)
	v_mfma_f32_32x32x16_bf16 v[32:47], v[164:167], v[180:183], v[32:47]
	ds_read_b64_tr_b16 v[176:177], v212 offset:45056
	ds_read_b64_tr_b16 v[178:179], v212 offset:47104
	v_exp_f32_e32 v131, v131
	v_sub_f32_e32 v132, v132, v229
	v_sub_f32_e32 v133, v133, v229
	v_sub_f32_e32 v134, v134, v229
	s_waitcnt lgkmcnt(12)
	v_mfma_f32_32x32x16_bf16 v[16:31], v[164:167], v[184:187], v[16:31]
	ds_read_b64_tr_b16 v[180:181], v213 offset:45056
	ds_read_b64_tr_b16 v[182:183], v213 offset:47104
	v_sub_f32_e32 v135, v135, v229
	v_exp_f32_e32 v132, v132
	v_exp_f32_e32 v133, v133
	v_exp_f32_e32 v134, v134
	v_exp_f32_e32 v135, v135
	s_waitcnt lgkmcnt(12)
	v_mfma_f32_32x32x16_bf16 v[0:15], v[164:167], v[188:191], v[0:15]
	ds_read_b64_tr_b16 v[184:185], v214 offset:45056
	ds_read_b64_tr_b16 v[186:187], v214 offset:47104
	v_pk_add_f32 v[254:255], v[128:129], v[130:131]
	v_cvt_pk_bf16_f32 v128, v128, v129
	v_cvt_pk_bf16_f32 v129, v130, v131
	v_sub_f32_e32 v136, v136, v229
	s_waitcnt lgkmcnt(12)
	v_mfma_f32_32x32x16_bf16 v[64:79], v[168:171], v[192:195], v[64:79]
	ds_read_b64_tr_b16 v[188:189], v215 offset:45056
	ds_read_b64_tr_b16 v[190:191], v215 offset:47104
	v_sub_f32_e32 v137, v137, v229
	v_sub_f32_e32 v138, v138, v229
	v_sub_f32_e32 v139, v139, v229
	v_exp_f32_e32 v136, v136
	v_exp_f32_e32 v137, v137
	s_waitcnt lgkmcnt(12)
	v_mfma_f32_32x32x16_bf16 v[32:47], v[168:171], v[196:199], v[32:47]
	v_add_u32_e32 v230, v236, v240
	ds_read_b128 v[192:195], v230
	v_exp_f32_e32 v138, v138
	v_exp_f32_e32 v139, v139
	v_pk_add_f32 v[254:255], v[254:255], v[132:133]
	v_pk_add_f32 v[254:255], v[254:255], v[134:135]
	s_waitcnt lgkmcnt(11)
	v_mfma_f32_32x32x16_bf16 v[16:31], v[168:171], v[200:203], v[16:31]
	v_add3_u32 v230, v237, v240, s51
	ds_read_b128 v[196:199], v230
	v_cvt_pk_bf16_f32 v130, v132, v133
	v_cvt_pk_bf16_f32 v131, v134, v135
	v_sub_f32_e32 v140, v140, v229
	v_sub_f32_e32 v141, v141, v229
	v_sub_f32_e32 v142, v142, v229
	s_waitcnt lgkmcnt(10)
	v_mfma_f32_32x32x16_bf16 v[0:15], v[168:171], v[204:207], v[0:15]
	v_add3_u32 v230, v237, v240, s51
	ds_read_b128 v[200:203], v230 offset:8192
	v_sub_f32_e32 v143, v143, v229
	v_exp_f32_e32 v140, v140
	v_exp_f32_e32 v141, v141
	v_exp_f32_e32 v142, v142
	s_waitcnt lgkmcnt(9)
	v_mfma_f32_32x32x16_bf16 v[64:79], v[172:175], v[176:179], v[64:79]
	v_add_u32_e32 v230, v236, v241
	ds_read_b128 v[204:207], v230
	v_exp_f32_e32 v143, v143
	v_pk_add_f32 v[254:255], v[254:255], v[136:137]
	v_pk_add_f32 v[254:255], v[254:255], v[138:139]
	v_cvt_pk_bf16_f32 v132, v136, v137
	v_cvt_pk_bf16_f32 v133, v138, v139
	s_waitcnt lgkmcnt(8)
	v_mfma_f32_32x32x16_bf16 v[32:47], v[172:175], v[180:183], v[32:47]
	v_sub_f32_e32 v144, v144, v229
	v_sub_f32_e32 v145, v145, v229
	v_sub_f32_e32 v146, v146, v229
	v_sub_f32_e32 v147, v147, v229
	s_waitcnt lgkmcnt(6)
	v_mfma_f32_32x32x16_bf16 v[16:31], v[172:175], v[184:187], v[16:31]
	v_exp_f32_e32 v144, v144
	v_exp_f32_e32 v145, v145
	v_exp_f32_e32 v146, v146
	v_exp_f32_e32 v147, v147
	v_pk_add_f32 v[254:255], v[254:255], v[140:141]
	s_waitcnt lgkmcnt(4)
	v_mfma_f32_32x32x16_bf16 v[0:15], v[172:175], v[188:191], v[0:15]
	v_pk_add_f32 v[254:255], v[254:255], v[142:143]
	v_cvt_pk_bf16_f32 v134, v140, v141
	v_cvt_pk_bf16_f32 v135, v142, v143
	v_sub_f32_e32 v148, v148, v229
	s_waitcnt lgkmcnt(2)
	v_mfma_f32_32x32x16_bf16 v[160:175], v[196:199], v[192:195], 0
	v_add3_u32 v230, v237, v241, s51
	ds_read_b128 v[196:199], v230
	v_sub_f32_e32 v149, v149, v229
	v_sub_f32_e32 v150, v150, v229
	v_sub_f32_e32 v151, v151, v229
	v_exp_f32_e32 v148, v148
	s_waitcnt lgkmcnt(2)
	v_mfma_f32_32x32x16_bf16 v[176:191], v[200:203], v[192:195], 0
	v_add3_u32 v230, v237, v241, s51
	ds_read_b128 v[200:203], v230 offset:8192
	v_add_u32_e32 v230, v236, v242
	ds_read_b128 v[192:195], v230
	v_exp_f32_e32 v149, v149
	v_exp_f32_e32 v150, v150
	v_exp_f32_e32 v151, v151
	v_pk_add_f32 v[254:255], v[254:255], v[144:145]
	v_pk_add_f32 v[254:255], v[254:255], v[146:147]
	s_waitcnt lgkmcnt(2)
	v_mfma_f32_32x32x16_bf16 v[160:175], v[196:199], v[204:207], v[160:175]
	v_add3_u32 v230, v237, v242, s51
	ds_read_b128 v[196:199], v230
	v_cvt_pk_bf16_f32 v136, v144, v145
	v_cvt_pk_bf16_f32 v137, v146, v147
	v_sub_f32_e32 v152, v152, v229
	v_sub_f32_e32 v153, v153, v229
	s_waitcnt lgkmcnt(2)
	v_mfma_f32_32x32x16_bf16 v[176:191], v[200:203], v[204:207], v[176:191]
	v_add3_u32 v230, v237, v242, s51
	ds_read_b128 v[200:203], v230 offset:8192
	v_add_u32_e32 v230, v236, v243
	ds_read_b128 v[204:207], v230
	v_sub_f32_e32 v154, v154, v229
	v_sub_f32_e32 v155, v155, v229
	v_exp_f32_e32 v152, v152
	v_exp_f32_e32 v153, v153
	v_exp_f32_e32 v154, v154
	s_waitcnt lgkmcnt(2)
	v_mfma_f32_32x32x16_bf16 v[160:175], v[196:199], v[192:195], v[160:175]
	v_add3_u32 v230, v237, v243, s51
	ds_read_b128 v[196:199], v230
	v_exp_f32_e32 v155, v155
	v_pk_add_f32 v[254:255], v[254:255], v[148:149]
	v_pk_add_f32 v[254:255], v[254:255], v[150:151]
	v_cvt_pk_bf16_f32 v138, v148, v149
	s_waitcnt lgkmcnt(2)
	v_mfma_f32_32x32x16_bf16 v[176:191], v[200:203], v[192:195], v[176:191]
	v_add3_u32 v230, v237, v243, s51
	ds_read_b128 v[200:203], v230 offset:8192
	v_cvt_pk_bf16_f32 v139, v150, v151
	v_sub_f32_e32 v156, v156, v229
	v_sub_f32_e32 v157, v157, v229
	v_sub_f32_e32 v158, v158, v229
	v_sub_f32_e32 v159, v159, v229
	s_waitcnt lgkmcnt(1)
	v_mfma_f32_32x32x16_bf16 v[160:175], v[196:199], v[204:207], v[160:175]
	v_exp_f32_e32 v156, v156
	v_exp_f32_e32 v157, v157
	v_exp_f32_e32 v158, v158
	v_exp_f32_e32 v159, v159
	s_waitcnt lgkmcnt(0)
	v_mfma_f32_32x32x16_bf16 v[176:191], v[200:203], v[204:207], v[176:191]
	v_pk_add_f32 v[254:255], v[254:255], v[152:153]
	v_pk_add_f32 v[254:255], v[254:255], v[154:155]
	v_cvt_pk_bf16_f32 v140, v152, v153
	v_cvt_pk_bf16_f32 v141, v154, v155
	s_nop 0
	v_pk_add_f32 v[254:255], v[254:255], v[156:157]
	v_pk_add_f32 v[254:255], v[254:255], v[158:159]
	v_cvt_pk_bf16_f32 v142, v156, v157
	v_cvt_pk_bf16_f32 v143, v158, v159
	v_add_f32_e32 v254, v254, v255
	v_mov_b32_e32 v255, v254
	s_nop 1
	v_permlane32_swap_b32_e32 v254, v255
	v_add_f32_e32 v254, v254, v255
	v_fma_f32 v208, v208, v228, v254
	s_branch .Lattn_tail

.Lattn_noresc1_d:
	ds_read_b64_tr_b16 v[188:189], v215 offset:36864
	ds_read_b64_tr_b16 v[190:191], v215 offset:38912
	ds_read_b64_tr_b16 v[192:193], v212 offset:40960
	ds_read_b64_tr_b16 v[194:195], v212 offset:43008
	ds_read_b64_tr_b16 v[196:197], v213 offset:40960
	ds_read_b64_tr_b16 v[198:199], v213 offset:43008
	ds_read_b64_tr_b16 v[200:201], v214 offset:40960
	ds_read_b64_tr_b16 v[202:203], v214 offset:43008
	v_sub_f32_e32 v128, v128, v229
	v_sub_f32_e32 v129, v129, v229
	v_sub_f32_e32 v130, v130, v229
	s_waitcnt lgkmcnt(12)
	v_mfma_f32_32x32x16_bf16 v[64:79], v[164:167], v[176:179], v[64:79]
	ds_read_b64_tr_b16 v[204:205], v215 offset:40960
	ds_read_b64_tr_b16 v[206:207], v215 offset:43008
	v_sub_f32_e32 v131, v131, v229
	v_exp_f32_e32 v128, v128
	v_exp_f32_e32 v129, v129
	v_exp_f32_e32 v130, v130
	v_exp_f32_e32 v131, v131
	v_sub_f32_e32 v132, v132, v229
	v_sub_f32_e32 v133, v133, v229
	s_waitcnt lgkmcnt(12)
	v_mfma_f32_32x32x16_bf16 v[32:47], v[164:167], v[180:183], v[32:47]
	ds_read_b64_tr_b16 v[176:177], v212 offset:45056
	ds_read_b64_tr_b16 v[178:179], v212 offset:47104
	v_sub_f32_e32 v134, v134, v229
	v_sub_f32_e32 v135, v135, v229
	v_exp_f32_e32 v132, v132
	v_exp_f32_e32 v133, v133
	v_exp_f32_e32 v134, v134
	v_exp_f32_e32 v135, v135
	v_pk_add_f32 v[254:255], v[128:129], v[130:131]
	v_cvt_pk_bf16_f32 v128, v128, v129
	s_waitcnt lgkmcnt(12)
	v_mfma_f32_32x32x16_bf16 v[16:31], v[164:167], v[184:187], v[16:31]
	ds_read_b64_tr_b16 v[180:181], v213 offset:45056
	ds_read_b64_tr_b16 v[182:183], v213 offset:47104
	v_cvt_pk_bf16_f32 v129, v130, v131
	v_sub_f32_e32 v136, v136, v229
	v_sub_f32_e32 v137, v137, v229
	v_sub_f32_e32 v138, v138, v229
	v_sub_f32_e32 v139, v139, v229
	v_exp_f32_e32 v136, v136
	v_exp_f32_e32 v137, v137
	v_exp_f32_e32 v138, v138
	s_waitcnt lgkmcnt(12)
	v_mfma_f32_32x32x16_bf16 v[0:15], v[164:167], v[188:191], v[0:15]
	ds_read_b64_tr_b16 v[184:185], v214 offset:45056
	ds_read_b64_tr_b16 v[186:187], v214 offset:47104
	v_exp_f32_e32 v139, v139
	v_pk_add_f32 v[254:255], v[254:255], v[132:133]
	v_pk_add_f32 v[254:255], v[254:255], v[134:135]
	v_cvt_pk_bf16_f32 v130, v132, v133
	v_cvt_pk_bf16_f32 v131, v134, v135
	v_sub_f32_e32 v140, v140, v229
	v_sub_f32_e32 v141, v141, v229
	s_waitcnt lgkmcnt(12)
	v_mfma_f32_32x32x16_bf16 v[64:79], v[168:171], v[192:195], v[64:79]
	ds_read_b64_tr_b16 v[188:189], v215 offset:45056
	ds_read_b64_tr_b16 v[190:191], v215 offset:47104
	v_sub_f32_e32 v142, v142, v229
	v_sub_f32_e32 v143, v143, v229
	v_exp_f32_e32 v140, v140
	v_exp_f32_e32 v141, v141
	v_exp_f32_e32 v142, v142
	v_exp_f32_e32 v143, v143
	v_pk_add_f32 v[254:255], v[254:255], v[136:137]
	v_pk_add_f32 v[254:255], v[254:255], v[138:139]
	s_waitcnt lgkmcnt(12)
	v_mfma_f32_32x32x16_bf16 v[32:47], v[168:171], v[196:199], v[32:47]
	v_cvt_pk_bf16_f32 v132, v136, v137
	v_cvt_pk_bf16_f32 v133, v138, v139
	v_sub_f32_e32 v144, v144, v229
	v_sub_f32_e32 v145, v145, v229
	v_sub_f32_e32 v146, v146, v229
	v_sub_f32_e32 v147, v147, v229
	v_exp_f32_e32 v144, v144
	v_exp_f32_e32 v145, v145
	s_waitcnt lgkmcnt(10)
	v_mfma_f32_32x32x16_bf16 v[16:31], v[168:171], v[200:203], v[16:31]
	v_exp_f32_e32 v146, v146
	v_exp_f32_e32 v147, v147
	v_pk_add_f32 v[254:255], v[254:255], v[140:141]
	v_pk_add_f32 v[254:255], v[254:255], v[142:143]
	v_cvt_pk_bf16_f32 v134, v140, v141
	v_cvt_pk_bf16_f32 v135, v142, v143
	v_sub_f32_e32 v148, v148, v229
	s_waitcnt lgkmcnt(8)
	v_mfma_f32_32x32x16_bf16 v[0:15], v[168:171], v[204:207], v[0:15]
	v_sub_f32_e32 v149, v149, v229
	v_sub_f32_e32 v150, v150, v229
	v_sub_f32_e32 v151, v151, v229
	v_exp_f32_e32 v148, v148
	v_exp_f32_e32 v149, v149
	v_exp_f32_e32 v150, v150
	v_exp_f32_e32 v151, v151
	v_pk_add_f32 v[254:255], v[254:255], v[144:145]
	s_waitcnt lgkmcnt(6)
	v_mfma_f32_32x32x16_bf16 v[64:79], v[172:175], v[176:179], v[64:79]
	v_pk_add_f32 v[254:255], v[254:255], v[146:147]
	v_cvt_pk_bf16_f32 v136, v144, v145
	v_cvt_pk_bf16_f32 v137, v146, v147
	v_sub_f32_e32 v152, v152, v229
	v_sub_f32_e32 v153, v153, v229
	v_sub_f32_e32 v154, v154, v229
	v_sub_f32_e32 v155, v155, v229
	v_exp_f32_e32 v152, v152
	s_waitcnt lgkmcnt(4)
	v_mfma_f32_32x32x16_bf16 v[32:47], v[172:175], v[180:183], v[32:47]
	v_exp_f32_e32 v153, v153
	v_exp_f32_e32 v154, v154
	v_exp_f32_e32 v155, v155
	v_pk_add_f32 v[254:255], v[254:255], v[148:149]
	v_pk_add_f32 v[254:255], v[254:255], v[150:151]
	v_cvt_pk_bf16_f32 v138, v148, v149
	v_cvt_pk_bf16_f32 v139, v150, v151
	v_sub_f32_e32 v156, v156, v229
	s_waitcnt lgkmcnt(2)
	v_mfma_f32_32x32x16_bf16 v[16:31], v[172:175], v[184:187], v[16:31]
	v_sub_f32_e32 v157, v157, v229
	v_sub_f32_e32 v158, v158, v229
	v_sub_f32_e32 v159, v159, v229
	v_exp_f32_e32 v156, v156
	v_exp_f32_e32 v157, v157
	v_exp_f32_e32 v158, v158
	v_exp_f32_e32 v159, v159
	s_waitcnt lgkmcnt(0)
	v_mfma_f32_32x32x16_bf16 v[0:15], v[172:175], v[188:191], v[0:15]
	v_pk_add_f32 v[254:255], v[254:255], v[152:153]
	v_pk_add_f32 v[254:255], v[254:255], v[154:155]
	v_cvt_pk_bf16_f32 v140, v152, v153
	v_cvt_pk_bf16_f32 v141, v154, v155
	s_nop 0
	v_pk_add_f32 v[254:255], v[254:255], v[156:157]
	v_pk_add_f32 v[254:255], v[254:255], v[158:159]
	v_cvt_pk_bf16_f32 v142, v156, v157
	v_cvt_pk_bf16_f32 v143, v158, v159
	v_add_f32_e32 v254, v254, v255
	v_mov_b32_e32 v255, v254
	s_nop 1
	v_permlane32_swap_b32_e32 v254, v255
	v_add_f32_e32 v254, v254, v255
	v_fma_f32 v208, v208, v228, v254
